# M3 retention: decay weights via min(lgf*d, -lgb*d) on the float distance (same products bit for bit): 5 instead of 11 VALU per element
# speedup vs baseline: 1.0038x; 1.0038x over previous
.LBB0_556:
	v_cndmask_b32_e64 v34, 0, 1, s[4:5]
	s_lshl_b32 s4, s10, 6
	v_cmp_ne_u32_e32 vcc, 1, v34
	v_or_b32_e32 v34, s4, v108
	v_lshl_add_u32 v152, v34, 7, s58
	v_add_u32_e32 v38, v152, v120
	ds_read_b128 v[34:37], v38 offset:16384
	ds_read_b128 v[50:53], v38 offset:20480
	v_add_u32_e32 v148, v152, v121
	s_waitcnt vmcnt(3) lgkmcnt(1)
	v_mfma_f32_32x32x16_bf16 v[34:49], v[34:37], v[78:81], 0
	ds_read_b128 v[144:147], v148 offset:16384
	ds_read_b128 v[148:151], v148 offset:20480
	s_waitcnt lgkmcnt(2)
	v_mfma_f32_32x32x16_bf16 v[50:65], v[50:53], v[78:81], 0
	s_waitcnt vmcnt(2) lgkmcnt(1)
	v_mfma_f32_32x32x16_bf16 v[34:49], v[144:147], v[74:77], v[34:49]
	s_waitcnt lgkmcnt(0)
	v_mfma_f32_32x32x16_bf16 v[50:65], v[148:151], v[74:77], v[50:65]
	v_add_u32_e32 v148, v152, v122
	ds_read_b128 v[144:147], v148 offset:16384
	ds_read_b128 v[148:151], v148 offset:20480
	s_waitcnt vmcnt(1) lgkmcnt(1)
	v_mfma_f32_32x32x16_bf16 v[34:49], v[144:147], v[70:73], v[34:49]
	s_waitcnt lgkmcnt(0)
	v_mfma_f32_32x32x16_bf16 v[50:65], v[148:151], v[70:73], v[50:65]
	v_add_u32_e32 v148, v152, v123
	ds_read_b128 v[144:147], v148 offset:16384
	ds_read_b128 v[148:151], v148 offset:20480
	s_waitcnt vmcnt(0) lgkmcnt(1)
	v_mfma_f32_32x32x16_bf16 v[34:49], v[144:147], v[66:69], v[34:49]
	v_or_b32_e32 v145, s4, v82
	s_waitcnt lgkmcnt(0)
	v_mfma_f32_32x32x16_bf16 v[50:65], v[148:151], v[66:69], v[50:65]
	v_sub_u32_e32 v166, v109, v145
	v_cvt_f32_i32_e32 v166, v166
	s_nop 7
	v_mov_b32_e32 v160, v166
	v_add_f32_e32 v161, 0xc2000000, v166
	v_pk_mul_f32 v[162:163], v[160:161], v[100:101] op_sel:[0,1] op_sel_hi:[1,1]
	v_pk_mul_f32 v[164:165], v[160:161], v[102:103] op_sel:[0,1] op_sel_hi:[1,1] neg_lo:[0,1] neg_hi:[0,1]
	v_min_f32_e32 v162, v162, v164
	v_min_f32_e32 v163, v163, v165
	v_exp_f32_e32 v162, v162
	v_exp_f32_e32 v163, v163
	v_mul_f32_e32 v144, v34, v162
	v_mul_f32_e32 v34, v50, v163
	v_add_f32_e32 v160, 0xbf800000, v166
	v_add_f32_e32 v161, 0xc2040000, v166
	v_pk_mul_f32 v[162:163], v[160:161], v[100:101] op_sel:[0,1] op_sel_hi:[1,1]
	v_pk_mul_f32 v[164:165], v[160:161], v[102:103] op_sel:[0,1] op_sel_hi:[1,1] neg_lo:[0,1] neg_hi:[0,1]
	v_min_f32_e32 v162, v162, v164
	v_min_f32_e32 v163, v163, v165
	v_exp_f32_e32 v162, v162
	v_exp_f32_e32 v163, v163
	v_mul_f32_e32 v50, v35, v162
	v_mul_f32_e32 v35, v51, v163
	v_add_f32_e32 v160, 0xc0000000, v166
	v_add_f32_e32 v161, 0xc2080000, v166
	v_pk_mul_f32 v[162:163], v[160:161], v[100:101] op_sel:[0,1] op_sel_hi:[1,1]
	v_pk_mul_f32 v[164:165], v[160:161], v[102:103] op_sel:[0,1] op_sel_hi:[1,1] neg_lo:[0,1] neg_hi:[0,1]
	v_min_f32_e32 v162, v162, v164
	v_min_f32_e32 v163, v163, v165
	v_exp_f32_e32 v162, v162
	v_exp_f32_e32 v163, v163
	v_mul_f32_e32 v51, v36, v162
	v_mul_f32_e32 v36, v52, v163
	v_add_f32_e32 v160, 0xc0400000, v166
	v_add_f32_e32 v161, 0xc20c0000, v166
	v_pk_mul_f32 v[162:163], v[160:161], v[100:101] op_sel:[0,1] op_sel_hi:[1,1]
	v_pk_mul_f32 v[164:165], v[160:161], v[102:103] op_sel:[0,1] op_sel_hi:[1,1] neg_lo:[0,1] neg_hi:[0,1]
	v_min_f32_e32 v162, v162, v164
	v_min_f32_e32 v163, v163, v165
	v_exp_f32_e32 v162, v162
	v_exp_f32_e32 v163, v163
	v_mul_f32_e32 v52, v37, v162
	v_mul_f32_e32 v37, v53, v163
	v_add_f32_e32 v160, 0xc1000000, v166
	v_add_f32_e32 v161, 0xc2200000, v166
	v_pk_mul_f32 v[162:163], v[160:161], v[100:101] op_sel:[0,1] op_sel_hi:[1,1]
	v_pk_mul_f32 v[164:165], v[160:161], v[102:103] op_sel:[0,1] op_sel_hi:[1,1] neg_lo:[0,1] neg_hi:[0,1]
	v_min_f32_e32 v162, v162, v164
	v_min_f32_e32 v163, v163, v165
	v_exp_f32_e32 v162, v162
	v_exp_f32_e32 v163, v163
	v_mul_f32_e32 v53, v38, v162
	v_mul_f32_e32 v38, v54, v163
	v_add_f32_e32 v160, 0xc1100000, v166
	v_add_f32_e32 v161, 0xc2240000, v166
	v_pk_mul_f32 v[162:163], v[160:161], v[100:101] op_sel:[0,1] op_sel_hi:[1,1]
	v_pk_mul_f32 v[164:165], v[160:161], v[102:103] op_sel:[0,1] op_sel_hi:[1,1] neg_lo:[0,1] neg_hi:[0,1]
	v_min_f32_e32 v162, v162, v164
	v_min_f32_e32 v163, v163, v165
	v_exp_f32_e32 v162, v162
	v_exp_f32_e32 v163, v163
	v_mul_f32_e32 v54, v39, v162
	v_mul_f32_e32 v39, v55, v163
	v_add_f32_e32 v160, 0xc1200000, v166
	v_add_f32_e32 v161, 0xc2280000, v166
	v_pk_mul_f32 v[162:163], v[160:161], v[100:101] op_sel:[0,1] op_sel_hi:[1,1]
	v_pk_mul_f32 v[164:165], v[160:161], v[102:103] op_sel:[0,1] op_sel_hi:[1,1] neg_lo:[0,1] neg_hi:[0,1]
	v_min_f32_e32 v162, v162, v164
	v_min_f32_e32 v163, v163, v165
	v_exp_f32_e32 v162, v162
	v_exp_f32_e32 v163, v163
	v_mul_f32_e32 v55, v40, v162
	v_mul_f32_e32 v40, v56, v163
	v_add_f32_e32 v160, 0xc1300000, v166
	v_add_f32_e32 v161, 0xc22c0000, v166
	v_pk_mul_f32 v[162:163], v[160:161], v[100:101] op_sel:[0,1] op_sel_hi:[1,1]
	v_pk_mul_f32 v[164:165], v[160:161], v[102:103] op_sel:[0,1] op_sel_hi:[1,1] neg_lo:[0,1] neg_hi:[0,1]
	v_min_f32_e32 v162, v162, v164
	v_min_f32_e32 v163, v163, v165
	v_exp_f32_e32 v162, v162
	v_exp_f32_e32 v163, v163
	v_mul_f32_e32 v56, v41, v162
	v_mul_f32_e32 v41, v57, v163
	v_add_f32_e32 v160, 0xc1800000, v166
	v_add_f32_e32 v161, 0xc2400000, v166
	v_pk_mul_f32 v[162:163], v[160:161], v[100:101] op_sel:[0,1] op_sel_hi:[1,1]
	v_pk_mul_f32 v[164:165], v[160:161], v[102:103] op_sel:[0,1] op_sel_hi:[1,1] neg_lo:[0,1] neg_hi:[0,1]
	v_min_f32_e32 v162, v162, v164
	v_min_f32_e32 v163, v163, v165
	v_exp_f32_e32 v162, v162
	v_exp_f32_e32 v163, v163
	v_mul_f32_e32 v57, v42, v162
	v_mul_f32_e32 v42, v58, v163
	v_add_f32_e32 v160, 0xc1880000, v166
	v_add_f32_e32 v161, 0xc2440000, v166
	v_pk_mul_f32 v[162:163], v[160:161], v[100:101] op_sel:[0,1] op_sel_hi:[1,1]
	v_pk_mul_f32 v[164:165], v[160:161], v[102:103] op_sel:[0,1] op_sel_hi:[1,1] neg_lo:[0,1] neg_hi:[0,1]
	v_min_f32_e32 v162, v162, v164
	v_min_f32_e32 v163, v163, v165
	v_exp_f32_e32 v162, v162
	v_exp_f32_e32 v163, v163
	v_mul_f32_e32 v43, v43, v162
	v_mul_f32_e32 v58, v59, v163
	v_add_f32_e32 v160, 0xc1900000, v166
	v_add_f32_e32 v161, 0xc2480000, v166
	v_pk_mul_f32 v[162:163], v[160:161], v[100:101] op_sel:[0,1] op_sel_hi:[1,1]
	v_pk_mul_f32 v[164:165], v[160:161], v[102:103] op_sel:[0,1] op_sel_hi:[1,1] neg_lo:[0,1] neg_hi:[0,1]
	v_min_f32_e32 v162, v162, v164
	v_min_f32_e32 v163, v163, v165
	v_exp_f32_e32 v162, v162
	v_exp_f32_e32 v163, v163
	v_mul_f32_e32 v59, v44, v162
	v_mul_f32_e32 v60, v60, v163
	v_add_f32_e32 v160, 0xc1980000, v166
	v_add_f32_e32 v161, 0xc24c0000, v166
	v_pk_mul_f32 v[162:163], v[160:161], v[100:101] op_sel:[0,1] op_sel_hi:[1,1]
	v_pk_mul_f32 v[164:165], v[160:161], v[102:103] op_sel:[0,1] op_sel_hi:[1,1] neg_lo:[0,1] neg_hi:[0,1]
	v_min_f32_e32 v162, v162, v164
	v_min_f32_e32 v163, v163, v165
	v_exp_f32_e32 v162, v162
	v_exp_f32_e32 v163, v163
	v_mul_f32_e32 v147, v45, v162
	v_mul_f32_e32 v61, v61, v163
	v_add_f32_e32 v160, 0xc1c00000, v166
	v_add_f32_e32 v161, 0xc2600000, v166
	v_pk_mul_f32 v[162:163], v[160:161], v[100:101] op_sel:[0,1] op_sel_hi:[1,1]
	v_pk_mul_f32 v[164:165], v[160:161], v[102:103] op_sel:[0,1] op_sel_hi:[1,1] neg_lo:[0,1] neg_hi:[0,1]
	v_min_f32_e32 v162, v162, v164
	v_min_f32_e32 v163, v163, v165
	v_exp_f32_e32 v162, v162
	v_exp_f32_e32 v163, v163
	v_mul_f32_e32 v146, v46, v162
	v_mul_f32_e32 v62, v62, v163
	v_add_f32_e32 v160, 0xc1c80000, v166
	v_add_f32_e32 v161, 0xc2640000, v166
	v_pk_mul_f32 v[162:163], v[160:161], v[100:101] op_sel:[0,1] op_sel_hi:[1,1]
	v_pk_mul_f32 v[164:165], v[160:161], v[102:103] op_sel:[0,1] op_sel_hi:[1,1] neg_lo:[0,1] neg_hi:[0,1]
	v_min_f32_e32 v162, v162, v164
	v_min_f32_e32 v163, v163, v165
	v_exp_f32_e32 v162, v162
	v_exp_f32_e32 v163, v163
	v_mul_f32_e32 v148, v47, v162
	v_mul_f32_e32 v63, v63, v163
	v_add_f32_e32 v160, 0xc1d00000, v166
	v_add_f32_e32 v161, 0xc2680000, v166
	v_pk_mul_f32 v[162:163], v[160:161], v[100:101] op_sel:[0,1] op_sel_hi:[1,1]
	v_pk_mul_f32 v[164:165], v[160:161], v[102:103] op_sel:[0,1] op_sel_hi:[1,1] neg_lo:[0,1] neg_hi:[0,1]
	v_min_f32_e32 v162, v162, v164
	v_min_f32_e32 v163, v163, v165
	v_exp_f32_e32 v162, v162
	v_exp_f32_e32 v163, v163
	v_mul_f32_e32 v149, v48, v162
	v_mul_f32_e32 v64, v64, v163
	v_add_f32_e32 v160, 0xc1d80000, v166
	v_add_f32_e32 v161, 0xc26c0000, v166
	v_pk_mul_f32 v[162:163], v[160:161], v[100:101] op_sel:[0,1] op_sel_hi:[1,1]
	v_pk_mul_f32 v[164:165], v[160:161], v[102:103] op_sel:[0,1] op_sel_hi:[1,1] neg_lo:[0,1] neg_hi:[0,1]
	v_min_f32_e32 v162, v162, v164
	v_min_f32_e32 v163, v163, v165
	v_exp_f32_e32 v162, v162
	v_exp_f32_e32 v163, v163
	v_mul_f32_e32 v145, v49, v162
	v_mul_f32_e32 v65, v65, v163
	v_cvt_pk_bf16_f32 v44, v144, v50
	v_cvt_pk_bf16_f32 v45, v51, v52
	v_cvt_pk_bf16_f32 v46, v53, v54
	v_cvt_pk_bf16_f32 v47, v55, v56
	v_cvt_pk_bf16_f32 v48, v57, v43
	v_cvt_pk_bf16_f32 v49, v59, v147
	v_cvt_pk_bf16_f32 v50, v146, v148
	v_cvt_pk_bf16_f32 v51, v149, v145
	v_cvt_pk_bf16_f32 v34, v34, v35
	v_cvt_pk_bf16_f32 v35, v36, v37
	v_cvt_pk_bf16_f32 v36, v38, v39
	v_cvt_pk_bf16_f32 v37, v40, v41
	v_cvt_pk_bf16_f32 v38, v42, v58
	v_cvt_pk_bf16_f32 v39, v60, v61
	v_cvt_pk_bf16_f32 v40, v62, v63
	v_cvt_pk_bf16_f32 v41, v64, v65
	v_lshl_add_u32 v42, s10, 13, v110
	ds_read_b64_tr_b16 v[52:53], v42 offset:0
	ds_read_b64_tr_b16 v[54:55], v42 offset:0x400
	ds_read_b64_tr_b16 v[56:57], v42 offset:0x800
	ds_read_b64_tr_b16 v[58:59], v42 offset:0xc00
	ds_read_b64_tr_b16 v[60:61], v42 offset:0x1000
	ds_read_b64_tr_b16 v[62:63], v42 offset:0x1400
	ds_read_b64_tr_b16 v[144:145], v42 offset:0x1800
	ds_read_b64_tr_b16 v[146:147], v42 offset:0x1c00
	s_waitcnt lgkmcnt(0)
	v_permlane32_swap_b32_e32 v44, v46
	v_permlane32_swap_b32_e32 v45, v47
	v_permlane32_swap_b32_e32 v48, v50
	v_permlane32_swap_b32_e32 v49, v51
	v_permlane32_swap_b32_e32 v34, v36
	v_permlane32_swap_b32_e32 v35, v37
	v_permlane32_swap_b32_e32 v38, v40
	v_permlane32_swap_b32_e32 v39, v41
	v_mfma_f32_32x32x16_bf16 v[18:33], v[52:55], v[44:47], v[18:33]
	ds_read_b64_tr_b16 v[52:53], v42 offset:0x200
	ds_read_b64_tr_b16 v[54:55], v42 offset:0x600
	v_mfma_f32_32x32x16_bf16 v[18:33], v[56:59], v[48:51], v[18:33]
	ds_read_b64_tr_b16 v[56:57], v42 offset:0xa00
	ds_read_b64_tr_b16 v[58:59], v42 offset:0xe00
	v_mfma_f32_32x32x16_bf16 v[18:33], v[60:63], v[34:37], v[18:33]
	ds_read_b64_tr_b16 v[60:61], v42 offset:0x1200
	ds_read_b64_tr_b16 v[62:63], v42 offset:0x1600
	v_mfma_f32_32x32x16_bf16 v[18:33], v[144:147], v[38:41], v[18:33]
	ds_read_b64_tr_b16 v[144:145], v42 offset:0x1a00
	ds_read_b64_tr_b16 v[146:147], v42 offset:0x1e00
	s_waitcnt lgkmcnt(0)
	v_mfma_f32_32x32x16_bf16 v[2:17], v[52:55], v[44:47], v[2:17]
	s_mov_b64 s[4:5], 0
	s_and_b64 vcc, exec, vcc
	s_mov_b32 s10, 1
	v_mfma_f32_32x32x16_bf16 v[2:17], v[56:59], v[48:51], v[2:17]
	v_mfma_f32_32x32x16_bf16 v[2:17], v[60:63], v[34:37], v[2:17]
	v_mfma_f32_32x32x16_bf16 v[2:17], v[144:147], v[38:41], v[2:17]
	s_cbranch_vccz .LBB0_556
	v_mul_f32_e32 v34, v101, v111
	v_exp_f32_e32 v50, v34
	v_mul_f32_e32 v34, v103, v112
	v_exp_f32_e32 v51, v34
	v_lshlrev_b32_e32 v35, 16, v78
	v_and_b32_e32 v36, 0xffff0000, v78
	v_mul_f32_e32 v34, v50, v35
	v_mul_f32_e32 v37, v50, v36
	v_mul_f32_e32 v36, v51, v36
	v_cvt_pk_bf16_f32 v34, v34, v37
	v_mul_f32_e32 v35, v51, v35
	v_cvt_pk_bf16_f32 v38, v35, v36
	v_lshlrev_b32_e32 v36, 16, v79
	v_and_b32_e32 v37, 0xffff0000, v79
	v_mul_f32_e32 v35, v50, v36
	v_mul_f32_e32 v39, v50, v37
	v_mul_f32_e32 v37, v51, v37
	v_cvt_pk_bf16_f32 v35, v35, v39
	v_mul_f32_e32 v36, v51, v36
	v_cvt_pk_bf16_f32 v39, v36, v37
	v_lshlrev_b32_e32 v37, 16, v80
	v_and_b32_e32 v40, 0xffff0000, v80
	v_mul_f32_e32 v36, v50, v37
	v_mul_f32_e32 v41, v50, v40
	v_cvt_pk_bf16_f32 v36, v36, v41
	v_mul_f32_e32 v37, v51, v37
	v_mul_f32_e32 v40, v51, v40
	v_lshlrev_b32_e32 v41, 16, v81
	v_and_b32_e32 v42, 0xffff0000, v81
	v_cvt_pk_bf16_f32 v40, v37, v40
	v_mul_f32_e32 v37, v50, v41
	v_mul_f32_e32 v43, v50, v42
	v_mul_f32_e32 v41, v51, v41
	v_mul_f32_e32 v42, v51, v42
	v_cvt_pk_bf16_f32 v37, v37, v43
	v_cvt_pk_bf16_f32 v41, v41, v42
	ds_read_b128 v[42:45], v134 offset:32768
	ds_read_b128 v[46:49], v134 offset:40960
	s_waitcnt lgkmcnt(1)
	v_mfma_f32_32x32x16_bf16 v[18:33], v[42:45], v[34:37], v[18:33]
	s_mov_b64 s[4:5], 0x1400
	s_waitcnt lgkmcnt(0)
	v_mfma_f32_32x32x16_bf16 v[18:33], v[46:49], v[38:41], v[18:33]
	ds_read_b128 v[42:45], v134 offset:36864
	ds_read_b128 v[46:49], v134 offset:45056
	s_waitcnt lgkmcnt(1)
	v_mfma_f32_32x32x16_bf16 v[2:17], v[42:45], v[34:37], v[2:17]
	v_lshlrev_b32_e32 v35, 16, v74
	v_and_b32_e32 v36, 0xffff0000, v74
	v_mul_f32_e32 v34, v50, v35
	v_mul_f32_e32 v37, v50, v36
	v_mul_f32_e32 v36, v51, v36
	v_cvt_pk_bf16_f32 v34, v34, v37
	v_mul_f32_e32 v35, v51, v35
	s_waitcnt lgkmcnt(0)
	v_mfma_f32_32x32x16_bf16 v[2:17], v[46:49], v[38:41], v[2:17]
	v_cvt_pk_bf16_f32 v38, v35, v36
	v_lshlrev_b32_e32 v36, 16, v75
	v_and_b32_e32 v37, 0xffff0000, v75
	v_mul_f32_e32 v35, v50, v36
	v_mul_f32_e32 v39, v50, v37
	v_mul_f32_e32 v37, v51, v37
	v_cvt_pk_bf16_f32 v35, v35, v39
	v_mul_f32_e32 v36, v51, v36
	v_cvt_pk_bf16_f32 v39, v36, v37
	v_lshlrev_b32_e32 v37, 16, v76
	v_and_b32_e32 v40, 0xffff0000, v76
	v_mul_f32_e32 v36, v50, v37
	v_mul_f32_e32 v41, v50, v40
	v_cvt_pk_bf16_f32 v36, v36, v41
	v_mul_f32_e32 v37, v51, v37
	v_mul_f32_e32 v40, v51, v40
	v_lshlrev_b32_e32 v41, 16, v77
	v_and_b32_e32 v42, 0xffff0000, v77
	v_cvt_pk_bf16_f32 v40, v37, v40
	v_mul_f32_e32 v37, v50, v41
	v_mul_f32_e32 v43, v50, v42
	v_mul_f32_e32 v41, v51, v41
	v_mul_f32_e32 v42, v51, v42
	v_cvt_pk_bf16_f32 v37, v37, v43
	v_cvt_pk_bf16_f32 v41, v41, v42
	ds_read_b128 v[42:45], v135 offset:32768
	ds_read_b128 v[46:49], v135 offset:40960
	s_waitcnt lgkmcnt(1)
	v_mfma_f32_32x32x16_bf16 v[18:33], v[42:45], v[34:37], v[18:33]
	s_waitcnt lgkmcnt(0)
	v_mfma_f32_32x32x16_bf16 v[18:33], v[46:49], v[38:41], v[18:33]
	ds_read_b128 v[42:45], v135 offset:36864
	ds_read_b128 v[46:49], v135 offset:45056
	s_waitcnt lgkmcnt(1)
	v_mfma_f32_32x32x16_bf16 v[2:17], v[42:45], v[34:37], v[2:17]
	v_lshlrev_b32_e32 v35, 16, v70
	v_and_b32_e32 v36, 0xffff0000, v70
	v_mul_f32_e32 v34, v50, v35
	v_mul_f32_e32 v37, v50, v36
	v_mul_f32_e32 v36, v51, v36
	v_cvt_pk_bf16_f32 v34, v34, v37
	v_mul_f32_e32 v35, v51, v35
	s_waitcnt lgkmcnt(0)
	v_mfma_f32_32x32x16_bf16 v[2:17], v[46:49], v[38:41], v[2:17]
	v_cvt_pk_bf16_f32 v38, v35, v36
	v_lshlrev_b32_e32 v36, 16, v71
	v_and_b32_e32 v37, 0xffff0000, v71
	v_mul_f32_e32 v35, v50, v36
	v_mul_f32_e32 v39, v50, v37
	v_mul_f32_e32 v37, v51, v37
	v_cvt_pk_bf16_f32 v35, v35, v39
	v_mul_f32_e32 v36, v51, v36
	v_cvt_pk_bf16_f32 v39, v36, v37
	v_lshlrev_b32_e32 v37, 16, v72
	v_and_b32_e32 v40, 0xffff0000, v72
	v_mul_f32_e32 v36, v50, v37
	v_mul_f32_e32 v41, v50, v40
	v_cvt_pk_bf16_f32 v36, v36, v41
	v_mul_f32_e32 v37, v51, v37
	v_mul_f32_e32 v40, v51, v40
	v_lshlrev_b32_e32 v41, 16, v73
	v_and_b32_e32 v42, 0xffff0000, v73
	v_cvt_pk_bf16_f32 v40, v37, v40
	v_mul_f32_e32 v37, v50, v41
	v_mul_f32_e32 v43, v50, v42
	v_mul_f32_e32 v41, v51, v41
	v_mul_f32_e32 v42, v51, v42
	v_cvt_pk_bf16_f32 v37, v37, v43
	v_cvt_pk_bf16_f32 v41, v41, v42
	ds_read_b128 v[42:45], v136 offset:32768
	ds_read_b128 v[46:49], v136 offset:40960
	s_waitcnt lgkmcnt(1)
	v_mfma_f32_32x32x16_bf16 v[18:33], v[42:45], v[34:37], v[18:33]
	s_waitcnt lgkmcnt(0)
	v_mfma_f32_32x32x16_bf16 v[18:33], v[46:49], v[38:41], v[18:33]
	ds_read_b128 v[42:45], v136 offset:36864
	ds_read_b128 v[46:49], v136 offset:45056
	s_waitcnt lgkmcnt(1)
	v_mfma_f32_32x32x16_bf16 v[2:17], v[42:45], v[34:37], v[2:17]
	v_lshlrev_b32_e32 v35, 16, v66
	v_and_b32_e32 v36, 0xffff0000, v66
	v_mul_f32_e32 v34, v50, v35
	v_mul_f32_e32 v37, v50, v36
	v_mul_f32_e32 v36, v51, v36
	v_cvt_pk_bf16_f32 v34, v34, v37
	v_mul_f32_e32 v35, v51, v35
	s_waitcnt lgkmcnt(0)
	v_mfma_f32_32x32x16_bf16 v[2:17], v[46:49], v[38:41], v[2:17]
	v_cvt_pk_bf16_f32 v38, v35, v36
	v_lshlrev_b32_e32 v36, 16, v67
	v_and_b32_e32 v37, 0xffff0000, v67
	v_mul_f32_e32 v35, v50, v36
	v_mul_f32_e32 v39, v50, v37
	v_mul_f32_e32 v37, v51, v37
	v_cvt_pk_bf16_f32 v35, v35, v39
	v_mul_f32_e32 v36, v51, v36
	v_cvt_pk_bf16_f32 v39, v36, v37
	v_lshlrev_b32_e32 v37, 16, v68
	v_and_b32_e32 v40, 0xffff0000, v68
	v_mul_f32_e32 v36, v50, v37
	v_mul_f32_e32 v41, v50, v40
	v_cvt_pk_bf16_f32 v36, v36, v41
	v_mul_f32_e32 v37, v51, v37
	v_mul_f32_e32 v40, v51, v40
	v_lshlrev_b32_e32 v41, 16, v69
	v_and_b32_e32 v42, 0xffff0000, v69
	v_cvt_pk_bf16_f32 v40, v37, v40
	v_mul_f32_e32 v37, v50, v41
	v_mul_f32_e32 v43, v50, v42
	v_mul_f32_e32 v41, v51, v41
	v_mul_f32_e32 v42, v51, v42
	v_cvt_pk_bf16_f32 v37, v37, v43
	v_cvt_pk_bf16_f32 v41, v41, v42
	ds_read_b128 v[42:45], v137 offset:32768
	ds_read_b128 v[46:49], v137 offset:40960
	s_waitcnt lgkmcnt(1)
	v_mfma_f32_32x32x16_bf16 v[18:33], v[42:45], v[34:37], v[18:33]
	s_waitcnt lgkmcnt(0)
	v_mfma_f32_32x32x16_bf16 v[18:33], v[46:49], v[38:41], v[18:33]
	ds_read_b128 v[42:45], v137 offset:36864
	ds_read_b128 v[46:49], v137 offset:45056
	s_waitcnt lgkmcnt(1)
	v_mfma_f32_32x32x16_bf16 v[2:17], v[42:45], v[34:37], v[2:17]
	v_lshl_add_u64 v[34:35], s[22:23], 1, v[106:107]
	v_lshlrev_b32_e32 v36, 1, v82
	v_mov_b32_e32 v37, v0
	v_lshl_add_u64 v[34:35], v[34:35], 0, v[36:37]
	v_lshl_add_u64 v[36:37], v[34:35], 0, s[4:5]
	v_add_co_u32_e32 v34, vcc, s78, v34
	s_lshl_b64 s[4:5], s[24:25], 2
	s_nop 0
	v_addc_co_u32_e32 v35, vcc, 0, v35, vcc
	global_load_dwordx2 v[80:81], v[34:35], off offset:1024
	global_load_dwordx2 v[76:77], v[36:37], off offset:16
	global_load_dwordx2 v[74:75], v[36:37], off offset:32
	global_load_dwordx2 v[72:73], v[36:37], off offset:48
	global_load_dwordx2 v[70:71], v[36:37], off offset:64
	global_load_dwordx2 v[68:69], v[36:37], off offset:80
	global_load_dwordx2 v[66:67], v[36:37], off offset:96
	global_load_dwordx2 v[64:65], v[36:37], off offset:112
	ds_read_b32 v34, v0 offset:640
	ds_read_b32 v35, v0 offset:644
	s_waitcnt lgkmcnt(2)
	v_mfma_f32_32x32x16_bf16 v[2:17], v[46:49], v[38:41], v[2:17]
	v_mul_f32_e32 v78, v19, v19
	v_fmac_f32_e32 v78, v18, v18
	s_waitcnt lgkmcnt(1)
	v_readfirstlane_b32 s11, v34
	s_waitcnt lgkmcnt(0)
	v_readfirstlane_b32 s10, v35
	s_add_u32 s11, s11, s4
	s_addc_u32 s10, s10, s5
	s_lshl_b64 s[4:5], s[22:23], 2
	s_add_u32 s4, s11, s4
	s_addc_u32 s5, s10, s5
	v_lshlrev_b32_e32 v34, 2, v82
	global_load_dwordx4 v[144:147], v34, s[4:5]
	global_load_dwordx4 v[58:61], v34, s[4:5] offset:32
	global_load_dwordx4 v[54:57], v34, s[4:5] offset:64
	global_load_dwordx4 v[50:53], v34, s[4:5] offset:96
	global_load_dwordx4 v[46:49], v34, s[4:5] offset:128
	global_load_dwordx4 v[42:45], v34, s[4:5] offset:160
	global_load_dwordx4 v[38:41], v34, s[4:5] offset:192
	s_nop 0
	global_load_dwordx4 v[34:37], v34, s[4:5] offset:224
	v_fmac_f32_e32 v78, v20, v20
	v_fmac_f32_e32 v78, v21, v21
	v_fmac_f32_e32 v78, v22, v22
	v_fmac_f32_e32 v78, v23, v23
	v_fmac_f32_e32 v78, v24, v24
	v_fmac_f32_e32 v78, v25, v25
	v_fmac_f32_e32 v78, v26, v26
	v_fmac_f32_e32 v78, v27, v27
	v_fmac_f32_e32 v78, v28, v28
	v_fmac_f32_e32 v78, v29, v29
	v_fmac_f32_e32 v78, v30, v30
	v_fmac_f32_e32 v78, v31, v31
	v_fmac_f32_e32 v78, v32, v32
	v_fmac_f32_e32 v78, v33, v33
	v_fmac_f32_e32 v78, v2, v2
	v_fmac_f32_e32 v78, v3, v3
	v_fmac_f32_e32 v78, v4, v4
	v_fmac_f32_e32 v78, v5, v5
	v_fmac_f32_e32 v78, v6, v6
	v_fmac_f32_e32 v78, v7, v7
	v_fmac_f32_e32 v78, v8, v8
	v_fmac_f32_e32 v78, v9, v9
	v_fmac_f32_e32 v78, v10, v10
	v_fmac_f32_e32 v78, v11, v11
	v_fmac_f32_e32 v78, v12, v12
	v_fmac_f32_e32 v78, v13, v13
	v_fmac_f32_e32 v78, v14, v14
	v_fmac_f32_e32 v78, v15, v15
	v_pk_mul_f32 v[62:63], v[16:17], v[16:17]
	s_and_b64 vcc, exec, s[20:21]
	v_add_f32_e32 v62, v78, v62
	v_add_f32_e32 v62, v62, v63
	v_mov_b32_e32 v63, v62
	s_nop 1
	v_permlane32_swap_b32_e32 v62, v63
	v_add_f32_e32 v62, v62, v63
	v_fmamk_f32 v62, v62, 0x3c800000, v210
	v_rsq_f32_e32 v78, v62
	v_lshlrev_b64 v[62:63], 10, v[104:105]
	v_lshl_add_u64 v[62:63], s[82:83], 0, v[62:63]
	v_lshl_add_u64 v[62:63], v[62:63], 0, s[22:23]
	v_mul_f32_e32 v78, 0x41800000, v78
	v_mul_f32_e32 v150, v78, v18
	v_lshl_add_u64 v[62:63], v[62:63], 0, v[84:85]
	s_waitcnt vmcnt(15)
	v_lshlrev_b32_e32 v105, 16, v80
	v_mul_f32_e32 v79, 0xbfb8aa3b, v105
	v_exp_f32_e32 v79, v79
	v_and_b32_e32 v107, 0xffff0000, v80
	v_mul_f32_e32 v18, 0xbfb8aa3b, v107
	v_exp_f32_e32 v18, v18
	v_add_f32_e32 v79, 1.0, v79
	v_rcp_f32_e32 v151, v79
	v_lshlrev_b32_e32 v149, 16, v81
	v_add_f32_e32 v18, 1.0, v18
	v_and_b32_e32 v81, 0xffff0000, v81
	s_waitcnt vmcnt(7)
	v_mov_b32_e32 v104, v144
	v_pk_mul_f32 v[104:105], v[150:151], v[104:105]
	v_mov_b32_e32 v106, v145
	v_mul_f32_e32 v79, v104, v105
	v_rcp_f32_e32 v105, v18
	v_mul_f32_e32 v104, v78, v19
	v_mov_b32_e32 v148, v146
	v_mov_b32_e32 v80, v147
	v_pk_mul_f32 v[18:19], v[104:105], v[106:107]
	v_mul_f32_e32 v106, v78, v22
	v_mul_f32_e32 v101, v18, v19
	v_mul_f32_e32 v18, 0xbfb8aa3b, v149
	v_exp_f32_e32 v18, v18
	v_lshlrev_b32_e32 v105, 16, v77
	s_waitcnt vmcnt(6)
	v_mov_b32_e32 v104, v60
	v_and_b32_e32 v77, 0xffff0000, v77
	v_add_f32_e32 v18, 1.0, v18
	v_rcp_f32_e32 v19, v18
	v_mul_f32_e32 v18, v78, v20
	s_waitcnt vmcnt(5)
	v_mov_b32_e32 v60, v57
	v_pk_mul_f32 v[18:19], v[18:19], v[148:149]
	s_nop 0
	v_mul_f32_e32 v20, v18, v19
	v_mul_f32_e32 v18, 0xbfb8aa3b, v81
	v_exp_f32_e32 v18, v18
	s_nop 0
	v_add_f32_e32 v18, 1.0, v18
	v_rcp_f32_e32 v19, v18
	v_mul_f32_e32 v18, v78, v21
	v_lshlrev_b32_e32 v21, 16, v76
	v_pk_mul_f32 v[18:19], v[18:19], v[80:81]
	s_nop 0
	v_mul_f32_e32 v19, v18, v19
	v_cvt_pk_fp8_f32 v18, v79, v101
	v_and_b32_e32 v81, 0xffff0000, v76
	v_mov_b32_e32 v80, v59
	v_mov_b32_e32 v76, v61
	v_cvt_pk_fp8_f32 v18, v20, v19 op_sel:[0,0,1]
	v_mul_f32_e32 v19, 0xbfb8aa3b, v21
	v_exp_f32_e32 v19, v19
	v_mov_b32_e32 v20, v58
	v_lshlrev_b32_e32 v59, 16, v75
	v_and_b32_e32 v61, 0xffff0000, v75
	v_add_f32_e32 v19, 1.0, v19
	v_rcp_f32_e32 v107, v19
	v_mov_b32_e32 v58, v56
	v_pk_mul_f32 v[20:21], v[106:107], v[20:21]
	s_nop 0
	v_mul_f32_e32 v19, v20, v21
	v_mul_f32_e32 v20, 0xbfb8aa3b, v81
	v_exp_f32_e32 v20, v20
	s_nop 0
	v_add_f32_e32 v20, 1.0, v20
	v_rcp_f32_e32 v21, v20
	v_mul_f32_e32 v20, v78, v23
	v_pk_mul_f32 v[20:21], v[20:21], v[80:81]
	s_nop 0
	v_mul_f32_e32 v22, v20, v21
	v_mul_f32_e32 v20, 0xbfb8aa3b, v105
	v_exp_f32_e32 v20, v20
	s_nop 0
	v_add_f32_e32 v20, 1.0, v20
	v_rcp_f32_e32 v21, v20
	v_mul_f32_e32 v20, v78, v24
	v_mov_b32_e32 v24, v55
	v_pk_mul_f32 v[20:21], v[20:21], v[104:105]
	s_nop 0
	v_mul_f32_e32 v23, v20, v21
	v_mul_f32_e32 v20, 0xbfb8aa3b, v77
	v_exp_f32_e32 v20, v20
	s_nop 0
	v_add_f32_e32 v20, 1.0, v20
	v_rcp_f32_e32 v21, v20
	v_mul_f32_e32 v20, v78, v25
	v_and_b32_e32 v25, 0xffff0000, v74
	v_pk_mul_f32 v[20:21], v[20:21], v[76:77]
	s_nop 0
	v_mul_f32_e32 v21, v20, v21
	v_cvt_pk_fp8_f32 v20, v19, v22
	v_mov_b32_e32 v22, v54
	v_mul_f32_e32 v54, v78, v30
	v_cvt_pk_fp8_f32 v20, v23, v21 op_sel:[0,0,1]
	v_lshlrev_b32_e32 v23, 16, v74
	v_mul_f32_e32 v19, 0xbfb8aa3b, v23
	v_exp_f32_e32 v19, v19
	v_mul_f32_e32 v74, v78, v26
	s_waitcnt vmcnt(4)
	v_mov_b32_e32 v26, v52
	v_add_f32_e32 v19, 1.0, v19
	v_rcp_f32_e32 v75, v19
	v_mul_f32_e32 v19, 0xbfb8aa3b, v25
	v_exp_f32_e32 v19, v19
	v_pk_mul_f32 v[22:23], v[74:75], v[22:23]
	s_nop 0
	v_mul_f32_e32 v21, v22, v23
	v_add_f32_e32 v19, 1.0, v19
	v_rcp_f32_e32 v23, v19
	v_mul_f32_e32 v19, 0xbfb8aa3b, v59
	v_exp_f32_e32 v19, v19
	v_mul_f32_e32 v22, v78, v27
	v_pk_mul_f32 v[22:23], v[22:23], v[24:25]
	v_lshlrev_b32_e32 v27, 16, v73
	v_add_f32_e32 v19, 1.0, v19
	v_mul_f32_e32 v24, v22, v23
	v_rcp_f32_e32 v23, v19
	v_mul_f32_e32 v19, 0xbfb8aa3b, v61
	v_exp_f32_e32 v19, v19
	v_mul_f32_e32 v22, v78, v28
	v_pk_mul_f32 v[22:23], v[22:23], v[58:59]
	v_mov_b32_e32 v28, v53
	v_add_f32_e32 v19, 1.0, v19
	v_mul_f32_e32 v25, v22, v23
	v_rcp_f32_e32 v23, v19
	v_mul_f32_e32 v22, v78, v29
	v_cvt_pk_fp8_f32 v19, v21, v24
	v_pk_mul_f32 v[22:23], v[22:23], v[60:61]
	v_mov_b32_e32 v24, v51
	v_mul_f32_e32 v22, v22, v23
	v_lshlrev_b32_e32 v23, 16, v72
	v_mul_f32_e32 v21, 0xbfb8aa3b, v23
	v_exp_f32_e32 v21, v21
	v_cvt_pk_fp8_f32 v19, v25, v22 op_sel:[0,0,1]
	v_and_b32_e32 v25, 0xffff0000, v72
	v_mov_b32_e32 v22, v50
	v_add_f32_e32 v21, 1.0, v21
	v_rcp_f32_e32 v55, v21
	v_mul_f32_e32 v21, 0xbfb8aa3b, v25
	v_exp_f32_e32 v21, v21
	v_and_b32_e32 v29, 0xffff0000, v73
	v_pk_mul_f32 v[22:23], v[54:55], v[22:23]
	v_permlane32_swap_b32_e32 v18, v19
	v_add_f32_e32 v21, 1.0, v21
	v_mul_f32_e32 v30, v22, v23
	v_rcp_f32_e32 v23, v21
	v_mul_f32_e32 v21, 0xbfb8aa3b, v27
	v_exp_f32_e32 v21, v21
	v_mul_f32_e32 v22, v78, v31
	v_pk_mul_f32 v[22:23], v[22:23], v[24:25]
	v_add_f32_e32 v21, 1.0, v21
	v_mul_f32_e32 v24, v22, v23
	v_rcp_f32_e32 v23, v21
	v_mul_f32_e32 v21, 0xbfb8aa3b, v29
	v_exp_f32_e32 v21, v21
	v_mul_f32_e32 v22, v78, v32
	v_pk_mul_f32 v[22:23], v[22:23], v[26:27]
	v_mul_f32_e32 v26, v78, v2
	v_add_f32_e32 v21, 1.0, v21
	v_mul_f32_e32 v25, v22, v23
	v_rcp_f32_e32 v23, v21
	v_cvt_pk_fp8_f32 v21, v30, v24
	v_mul_f32_e32 v22, v78, v33
	v_pk_mul_f32 v[22:23], v[22:23], v[28:29]
	s_waitcnt vmcnt(3)
	v_mov_b32_e32 v24, v49
	v_mul_f32_e32 v22, v22, v23
	v_cvt_pk_fp8_f32 v21, v25, v22 op_sel:[0,0,1]
	v_lshlrev_b32_e32 v23, 16, v71
	v_mov_b32_e32 v22, v48
	v_and_b32_e32 v25, 0xffff0000, v71
	v_permlane32_swap_b32_e32 v20, v21
	global_store_dwordx4 v[62:63], v[18:21], off offset:768
	s_nop 1
	v_lshlrev_b32_e32 v19, 16, v70
	v_mul_f32_e32 v18, 0xbfb8aa3b, v19
	v_exp_f32_e32 v18, v18
	v_and_b32_e32 v21, 0xffff0000, v70
	v_mul_f32_e32 v2, 0xbfb8aa3b, v21
	v_exp_f32_e32 v2, v2
	v_add_f32_e32 v18, 1.0, v18
	v_rcp_f32_e32 v27, v18
	v_mov_b32_e32 v18, v46
	v_add_f32_e32 v2, 1.0, v2
	v_mov_b32_e32 v20, v47
	v_pk_mul_f32 v[18:19], v[26:27], v[18:19]
	s_nop 0
	v_mul_f32_e32 v26, v18, v19
	v_rcp_f32_e32 v19, v2
	v_mul_f32_e32 v18, v78, v3
	v_pk_mul_f32 v[2:3], v[18:19], v[20:21]
	s_nop 0
	v_mul_f32_e32 v18, v2, v3
	v_mul_f32_e32 v2, 0xbfb8aa3b, v23
	v_exp_f32_e32 v2, v2
	v_and_b32_e32 v19, 0xffff0000, v68
	v_lshlrev_b32_e32 v21, 16, v69
	s_waitcnt vmcnt(3)
	v_mov_b32_e32 v20, v44
	v_add_f32_e32 v2, 1.0, v2
	v_rcp_f32_e32 v3, v2
	v_mul_f32_e32 v2, v78, v4
	v_pk_mul_f32 v[2:3], v[2:3], v[22:23]
	s_nop 0
	v_mul_f32_e32 v4, v2, v3
	v_mul_f32_e32 v2, 0xbfb8aa3b, v25
	v_exp_f32_e32 v2, v2
	v_and_b32_e32 v23, 0xffff0000, v69
	v_mov_b32_e32 v22, v45
	v_add_f32_e32 v2, 1.0, v2
	v_rcp_f32_e32 v3, v2
	v_mul_f32_e32 v2, v78, v5
	v_lshlrev_b32_e32 v5, 16, v68
	v_pk_mul_f32 v[2:3], v[2:3], v[24:25]
	s_nop 0
	v_mul_f32_e32 v3, v2, v3
	v_cvt_pk_fp8_f32 v2, v26, v18
	v_mul_f32_e32 v24, v78, v6
	v_mov_b32_e32 v18, v43
	v_cvt_pk_fp8_f32 v2, v4, v3 op_sel:[0,0,1]
	v_mul_f32_e32 v3, 0xbfb8aa3b, v5
	v_exp_f32_e32 v3, v3
	v_mov_b32_e32 v4, v42
	v_add_f32_e32 v3, 1.0, v3
	v_rcp_f32_e32 v25, v3
	s_nop 0
	v_pk_mul_f32 v[4:5], v[24:25], v[4:5]
	s_nop 0
	v_mul_f32_e32 v3, v4, v5
	v_mul_f32_e32 v4, 0xbfb8aa3b, v19
	v_exp_f32_e32 v4, v4
	s_nop 0
	v_add_f32_e32 v4, 1.0, v4
	v_rcp_f32_e32 v5, v4
	v_mul_f32_e32 v4, v78, v7
	v_pk_mul_f32 v[4:5], v[4:5], v[18:19]
	s_nop 0
	v_mul_f32_e32 v6, v4, v5
	v_mul_f32_e32 v4, 0xbfb8aa3b, v21
	v_exp_f32_e32 v4, v4
	v_lshlrev_b32_e32 v19, 16, v67
	s_waitcnt vmcnt(2)
	v_mov_b32_e32 v18, v40
	v_add_f32_e32 v4, 1.0, v4
	v_rcp_f32_e32 v5, v4
	v_mul_f32_e32 v4, v78, v8
	v_mov_b32_e32 v8, v39
	v_pk_mul_f32 v[4:5], v[4:5], v[20:21]
	s_nop 0
	v_mul_f32_e32 v7, v4, v5
	v_mul_f32_e32 v4, 0xbfb8aa3b, v23
	v_exp_f32_e32 v4, v4
	v_and_b32_e32 v21, 0xffff0000, v67
	v_mov_b32_e32 v20, v41
	v_add_f32_e32 v4, 1.0, v4
	v_rcp_f32_e32 v5, v4
	v_mul_f32_e32 v4, v78, v9
	v_and_b32_e32 v9, 0xffff0000, v66
	v_pk_mul_f32 v[4:5], v[4:5], v[22:23]
	s_nop 0
	v_mul_f32_e32 v5, v4, v5
	v_cvt_pk_fp8_f32 v4, v3, v6
	v_mul_f32_e32 v22, v78, v10
	v_mov_b32_e32 v6, v38
	s_waitcnt vmcnt(1)
	v_mov_b32_e32 v10, v36
	v_cvt_pk_fp8_f32 v4, v7, v5 op_sel:[0,0,1]
	v_lshlrev_b32_e32 v7, 16, v66
	v_mul_f32_e32 v3, 0xbfb8aa3b, v7
	v_exp_f32_e32 v3, v3
	s_nop 0
	v_add_f32_e32 v3, 1.0, v3
	v_rcp_f32_e32 v23, v3
	v_mul_f32_e32 v3, 0xbfb8aa3b, v9
	v_exp_f32_e32 v3, v3
	v_pk_mul_f32 v[6:7], v[22:23], v[6:7]
	s_nop 0
	v_mul_f32_e32 v5, v6, v7
	v_add_f32_e32 v3, 1.0, v3
	v_rcp_f32_e32 v7, v3
	v_mul_f32_e32 v3, 0xbfb8aa3b, v19
	v_exp_f32_e32 v3, v3
	v_mul_f32_e32 v6, v78, v11
	v_pk_mul_f32 v[6:7], v[6:7], v[8:9]
	v_lshlrev_b32_e32 v11, 16, v65
	v_add_f32_e32 v3, 1.0, v3
	v_mul_f32_e32 v8, v6, v7
	v_rcp_f32_e32 v7, v3
	v_mul_f32_e32 v3, 0xbfb8aa3b, v21
	v_exp_f32_e32 v3, v3
	v_mul_f32_e32 v6, v78, v12
	v_pk_mul_f32 v[6:7], v[6:7], v[18:19]
	v_mul_f32_e32 v18, v78, v14
	v_add_f32_e32 v3, 1.0, v3
	v_mul_f32_e32 v9, v6, v7
	v_rcp_f32_e32 v7, v3
	v_mul_f32_e32 v6, v78, v13
	v_cvt_pk_fp8_f32 v3, v5, v8
	v_pk_mul_f32 v[6:7], v[6:7], v[20:21]
	v_mov_b32_e32 v8, v35
	v_mul_f32_e32 v6, v6, v7
	v_lshlrev_b32_e32 v7, 16, v64
	v_mul_f32_e32 v5, 0xbfb8aa3b, v7
	v_exp_f32_e32 v5, v5
	v_cvt_pk_fp8_f32 v3, v9, v6 op_sel:[0,0,1]
	v_and_b32_e32 v9, 0xffff0000, v64
	v_mov_b32_e32 v6, v34
	v_add_f32_e32 v5, 1.0, v5
	v_rcp_f32_e32 v19, v5
	v_mul_f32_e32 v5, 0xbfb8aa3b, v9
	v_exp_f32_e32 v5, v5
	v_and_b32_e32 v13, 0xffff0000, v65
	v_pk_mul_f32 v[6:7], v[18:19], v[6:7]
	v_mov_b32_e32 v12, v37
	v_add_f32_e32 v5, 1.0, v5
	v_mul_f32_e32 v14, v6, v7
	v_rcp_f32_e32 v7, v5
	v_mul_f32_e32 v5, 0xbfb8aa3b, v11
	v_exp_f32_e32 v5, v5
	v_mul_f32_e32 v6, v78, v15
	v_pk_mul_f32 v[6:7], v[6:7], v[8:9]
	v_permlane32_swap_b32_e32 v2, v3
	v_add_f32_e32 v5, 1.0, v5
	v_mul_f32_e32 v8, v6, v7
	v_rcp_f32_e32 v7, v5
	v_mul_f32_e32 v5, 0xbfb8aa3b, v13
	v_exp_f32_e32 v5, v5
	v_mul_f32_e32 v6, v78, v16
	v_pk_mul_f32 v[6:7], v[6:7], v[10:11]
	v_add_f32_e32 v5, 1.0, v5
	v_mul_f32_e32 v9, v6, v7
	v_rcp_f32_e32 v7, v5
	v_cvt_pk_fp8_f32 v5, v14, v8
	v_mul_f32_e32 v6, v78, v17
	v_pk_mul_f32 v[6:7], v[6:7], v[12:13]
	s_nop 0
	v_mul_f32_e32 v6, v6, v7
	v_cvt_pk_fp8_f32 v5, v9, v6 op_sel:[0,0,1]
	s_nop 1
	v_permlane32_swap_b32_e32 v4, v5
	global_store_dwordx4 v[62:63], v[2:5], off offset:800
	s_cbranch_vccz .LBB0_550
	s_waitcnt vmcnt(0)
	s_barrier
	s_and_saveexec_b64 s[4:5], s[0:1]
	s_cbranch_execz .LBB0_549
	s_mov_b64 s[10:11], exec
	v_mbcnt_lo_u32_b32 v2, s10, 0
	buffer_wbl2 sc1
	s_waitcnt vmcnt(0)
	s_waitcnt vmcnt(0)
	v_mbcnt_hi_u32_b32 v2, s11, v2
	v_cmp_eq_u32_e32 vcc, 0, v2
	s_and_b64 s[14:15], exec, vcc
	s_mov_b64 exec, s[14:15]
	s_cbranch_execz .LBB0_549
	s_bcnt1_i32_b64 s10, s[10:11]
	v_mov_b32_e32 v2, s10
	global_atomic_add v0, v2, s[84:85]
	s_branch .LBB0_549
